# V table bytes = 16*hi + lo + 8 (signed); sweep V low dots use raw bytes, high dots masked, token weight sum by one extra dot; exact recovery once per pass; weight LDS read hoisted
# speedup vs baseline: 1.0763x; 1.0046x over previous
; __device__ __forceinline__ unsigned q4(float x) { return (unsigned)(int)fminf(fmaxf(rintf(x), -7.0f), 7.0f) & 0xfu; }
; __device__ __forceinline__ void cvt_table_i4(const float* src, unsigned char* dst, float* scl, float scl_mul, int gw, int ngw, int lane) {
;     for (int row = gw; row < 16384; row += ngw) {
;         const f32x4* sp = (const f32x4*)(src + (size_t)row * 1024 + 16 * lane);
;         const f32x4 a0 = sp[0], a1 = sp[1], a2 = sp[2], a3 = sp[3];
;         float ss = ((a0.x * a0.x + a0.y * a0.y) + (a0.z * a0.z + a0.w * a0.w)) + ((a1.x * a1.x + a1.y * a1.y) + (a1.z * a1.z + a1.w * a1.w))
;                  + ((a2.x * a2.x + a2.y * a2.y) + (a2.z * a2.z + a2.w * a2.w)) + ((a3.x * a3.x + a3.y * a3.y) + (a3.z * a3.z + a3.w * a3.w));
;         ss = wave_sum(ss);
;         const float step = fmaxf(0.35f * sqrtf(ss * (1.0f / 1024.0f)), 1e-30f), q = 1.0f / step;
;         v2u o;
;         o.x = (q4(a0.x * q) | (q4(a1.x * q) << 4)) | ((q4(a0.y * q) | (q4(a1.y * q) << 4)) << 8) | ((q4(a0.z * q) | (q4(a1.z * q) << 4)) << 16) | ((q4(a0.w * q) | (q4(a1.w * q) << 4)) << 24);
;         o.y = (q4(a2.x * q) | (q4(a3.x * q) << 4)) | ((q4(a2.y * q) | (q4(a3.y * q) << 4)) << 8) | ((q4(a2.z * q) | (q4(a3.z * q) << 4)) << 16) | ((q4(a2.w * q) | (q4(a3.w * q) << 4)) << 24);
;         *(v2u*)(dst + (size_t)row * 512 + 8 * lane) = o;
;         if (lane == 0) scl[row] = step * scl_mul;
;     }
; }
.LBB0_1973:
	global_load_dwordx4 v[8:11], v[4:5], off offset:-32
	global_load_dwordx4 v[12:15], v[4:5], off offset:-16
	global_load_dwordx4 v[20:23], v[4:5], off
	global_load_dwordx4 v[24:27], v[4:5], off offset:16
	s_waitcnt vmcnt(0)
	v_mul_f32_e32 v7, v9, v9
	v_mul_f32_e32 v16, v11, v11
	v_mul_f32_e32 v17, v13, v13
	v_mul_f32_e32 v28, v15, v15
	v_mul_f32_e32 v29, v21, v21
	v_mul_f32_e32 v30, v23, v23
	v_fmac_f32_e32 v7, v8, v8
	v_fmac_f32_e32 v16, v10, v10
	v_fmac_f32_e32 v17, v12, v12
	v_fmac_f32_e32 v28, v14, v14
	v_mul_f32_e32 v31, v25, v25
	v_mul_f32_e32 v32, v27, v27
	v_fmac_f32_e32 v29, v20, v20
	v_fmac_f32_e32 v30, v22, v22
	v_add_f32_e32 v7, v7, v16
	v_add_f32_e32 v16, v17, v28
	v_fmac_f32_e32 v31, v24, v24
	v_fmac_f32_e32 v32, v26, v26
	v_add_f32_e32 v17, v29, v30
	v_add_f32_e32 v7, v7, v16
	v_add_f32_e32 v28, v31, v32
	v_add_f32_e32 v7, v7, v17
	v_add_f32_e32 v7, v7, v28
	s_nop 1
	v_add_f32_dpp v7, v7, v7 quad_perm:[1,0,3,2] row_mask:0xf bank_mask:0xf bound_ctrl:1
	s_nop 1
	v_add_f32_dpp v7, v7, v7 quad_perm:[2,3,0,1] row_mask:0xf bank_mask:0xf bound_ctrl:1
	s_nop 1
	v_add_f32_dpp v7, v7, v7 row_half_mirror row_mask:0xf bank_mask:0xf bound_ctrl:1
	s_nop 1
	v_add_f32_dpp v7, v7, v7 row_mirror row_mask:0xf bank_mask:0xf bound_ctrl:1
	v_mov_b32_e32 v16, v7
	s_nop 1
	v_permlane16_swap_b32_e32 v7, v16
	v_add_f32 v7, v7, v16
	s_nop 1
	s_nop 0
	v_mov_b32_e32 v16, v7
	s_nop 1
	v_permlane32_swap_b32_e32 v7, v16
	v_add_f32 v7, v7, v16
	s_nop 0
	v_mul_f32_e32 v7, 0x3a800000, v7
	v_mul_f32_e32 v16, 0x4f800000, v7
	v_cmp_gt_f32_e32 vcc, s3, v7
	s_nop 1
	v_cndmask_b32_e32 v7, v7, v16, vcc
	v_sqrt_f32_e32 v16, v7
	s_nop 0
	v_add_u32_e32 v17, -1, v16
	v_add_u32_e32 v28, 1, v16
	v_fma_f32 v29, -v17, v16, v7
	v_fma_f32 v30, -v28, v16, v7
	v_cmp_ge_f32_e64 s[0:1], 0, v29
	s_nop 1
	v_cndmask_b32_e64 v16, v16, v17, s[0:1]
	v_cmp_lt_f32_e64 s[0:1], 0, v30
	s_nop 1
	v_cndmask_b32_e64 v16, v16, v28, s[0:1]
	v_mul_f32_e32 v17, 0x37800000, v16
	v_cndmask_b32_e32 v16, v16, v17, vcc
	v_cmp_class_f32_e32 vcc, v7, v1
	s_nop 1
	v_cndmask_b32_e32 v7, v16, v7, vcc
	v_mul_f32_e32 v7, 0x3eb33333, v7
	v_max_f32_e32 v7, 0xda24260, v7
	v_div_scale_f32 v16, s[0:1], v7, v7, 1.0
	v_rcp_f32_e32 v17, v16
	v_div_scale_f32 v28, vcc, 1.0, v7, 1.0
	v_fma_f32 v29, -v16, v17, 1.0
	v_fmac_f32_e32 v17, v29, v17
	v_mul_f32_e32 v29, v28, v17
	v_fma_f32 v30, -v16, v29, v28
	v_fmac_f32_e32 v29, v30, v17
	v_fma_f32 v16, -v16, v29, v28
	v_div_fmas_f32 v16, v16, v17, v29
	v_div_fixup_f32 v16, v16, v7, 1.0
	v_mul_f32_e32 v8, v8, v16
	v_mul_f32_e32 v9, v9, v16
	v_mul_f32_e32 v10, v10, v16
	v_mul_f32_e32 v11, v11, v16
	v_mul_f32_e32 v12, v12, v16
	v_mul_f32_e32 v13, v13, v16
	v_mul_f32_e32 v14, v14, v16
	v_mul_f32_e32 v15, v15, v16
	v_mul_f32_e32 v20, v20, v16
	v_mul_f32_e32 v21, v21, v16
	v_mul_f32_e32 v22, v22, v16
	v_mul_f32_e32 v23, v23, v16
	v_mul_f32_e32 v24, v24, v16
	v_mul_f32_e32 v25, v25, v16
	v_mul_f32_e32 v26, v26, v16
	v_mul_f32_e32 v27, v27, v16
	v_rndne_f32_e32 v8, v8
	v_rndne_f32_e32 v9, v9
	v_rndne_f32_e32 v10, v10
	v_rndne_f32_e32 v11, v11
	v_rndne_f32_e32 v12, v12
	v_rndne_f32_e32 v13, v13
	v_rndne_f32_e32 v14, v14
	v_rndne_f32_e32 v15, v15
	v_rndne_f32_e32 v20, v20
	v_rndne_f32_e32 v21, v21
	v_rndne_f32_e32 v22, v22
	v_rndne_f32_e32 v23, v23
	v_rndne_f32_e32 v24, v24
	v_rndne_f32_e32 v25, v25
	v_rndne_f32_e32 v26, v26
	v_rndne_f32_e32 v27, v27
	v_med3_f32 v8, v8, s13, v6
	v_med3_f32 v9, v9, s13, v6
	v_med3_f32 v10, v10, s13, v6
	v_med3_f32 v11, v11, s13, v6
	v_med3_f32 v12, v12, s13, v6
	v_med3_f32 v13, v13, s13, v6
	v_med3_f32 v14, v14, s13, v6
	v_med3_f32 v15, v15, s13, v6
	v_med3_f32 v20, v20, s13, v6
	v_med3_f32 v21, v21, s13, v6
	v_med3_f32 v22, v22, s13, v6
	v_med3_f32 v23, v23, s13, v6
	v_med3_f32 v24, v24, s13, v6
	v_med3_f32 v25, v25, s13, v6
	v_med3_f32 v26, v26, s13, v6
	v_med3_f32 v27, v27, s13, v6
	v_fmamk_f32 v8, v12, 0x41800000, v8
	v_fmamk_f32 v20, v24, 0x41800000, v20
	v_fmamk_f32 v9, v13, 0x41800000, v9
	v_fmamk_f32 v21, v25, 0x41800000, v21
	v_fmamk_f32 v10, v14, 0x41800000, v10
	v_fmamk_f32 v22, v26, 0x41800000, v22
	v_fmamk_f32 v11, v15, 0x41800000, v11
	v_fmamk_f32 v23, v27, 0x41800000, v23
	v_add_f32_e32 v8, 0x41000000, v8
	v_add_f32_e32 v20, 0x41000000, v20
	v_add_f32_e32 v9, 0x41000000, v9
	v_add_f32_e32 v21, 0x41000000, v21
	v_add_f32_e32 v10, 0x41000000, v10
	v_add_f32_e32 v22, 0x41000000, v22
	v_add_f32_e32 v11, 0x41000000, v11
	v_add_f32_e32 v23, 0x41000000, v23
	v_cvt_i32_f32_e32 v12, v8
	v_cvt_i32_f32_e32 v13, v20
	v_cvt_i32_f32_sdwa v12, v9 dst_sel:BYTE_1 dst_unused:UNUSED_PRESERVE src0_sel:DWORD
	v_cvt_i32_f32_sdwa v13, v21 dst_sel:BYTE_1 dst_unused:UNUSED_PRESERVE src0_sel:DWORD
	v_cvt_i32_f32_sdwa v12, v10 dst_sel:BYTE_2 dst_unused:UNUSED_PRESERVE src0_sel:DWORD
	v_cvt_i32_f32_sdwa v13, v22 dst_sel:BYTE_2 dst_unused:UNUSED_PRESERVE src0_sel:DWORD
	v_cvt_i32_f32_sdwa v12, v11 dst_sel:BYTE_3 dst_unused:UNUSED_PRESERVE src0_sel:DWORD
	v_cvt_i32_f32_sdwa v13, v23 dst_sel:BYTE_3 dst_unused:UNUSED_PRESERVE src0_sel:DWORD
	s_nop 0
	global_store_dwordx2 v[2:3], v[12:13], off
	s_and_saveexec_b64 s[0:1], s[4:5]
	s_cbranch_execz .LBB0_1972
	v_mul_f32_e32 v7, 0x3d800000, v7
	global_store_dword v19, v7, s[6:7]
	s_branch .LBB0_1972

; #define PE_WAIT4U(S, cntstr) asm volatile("s_waitcnt " cntstr : "+v"(ru4[S][0]), "+v"(ru4[S][1]), "+v"(ru4[S][2]), "+v"(ru4[S][3]) :: "memory")
;     ...
; #pragma unroll
;         for (int q = 0; q < PE_RD; ++q) PE_WAIT4U(q, "vmcnt(0)");
;         PE_FLUSH();
.LBB0_2677:
	v_cvt_f32_i32_e32 v54, v54
	v_cvt_f32_i32_e32 v55, v55
	v_cvt_f32_i32_e32 v56, v56
	v_cvt_f32_i32_e32 v57, v57
	v_cvt_f32_i32_e32 v58, v58
	v_cvt_f32_i32_e32 v59, v59
	v_cvt_f32_i32_e32 v60, v60
	v_cvt_f32_i32_e32 v61, v61
	v_cvt_f32_i32_e32 v62, v62
	v_cvt_f32_i32_e32 v63, v63
	v_cvt_f32_i32_e32 v64, v64
	v_cvt_f32_i32_e32 v65, v65
	v_cvt_f32_i32_e32 v66, v66
	v_cvt_f32_i32_e32 v67, v67
	v_cvt_f32_i32_e32 v68, v68
	v_cvt_f32_i32_e32 v69, v69
	v_cvt_f32_i32_e32 v36, v36
	v_cvt_f32_i32_e32 v37, v37
	v_cvt_f32_i32_e32 v38, v38
	v_cvt_f32_i32_e32 v39, v39
	v_cvt_f32_i32_e32 v40, v40
	v_cvt_f32_i32_e32 v41, v41
	v_cvt_f32_i32_e32 v42, v42
	v_cvt_f32_i32_e32 v43, v43
	v_cvt_f32_i32_e32 v44, v44
	v_cvt_f32_i32_e32 v45, v45
	v_cvt_f32_i32_e32 v46, v46
	v_cvt_f32_i32_e32 v47, v47
	v_cvt_f32_i32_e32 v50, v50
	v_cvt_f32_i32_e32 v51, v51
	v_cvt_f32_i32_e32 v52, v52
	v_cvt_f32_i32_e32 v53, v53
	v_cvt_f32_i32_e32 v20, v20
	v_cvt_f32_i32_e32 v21, v21
	v_cvt_f32_i32_e32 v22, v22
	v_cvt_f32_i32_e32 v23, v23
	v_cvt_f32_i32_e32 v24, v24
	v_cvt_f32_i32_e32 v25, v25
	v_cvt_f32_i32_e32 v26, v26
	v_cvt_f32_i32_e32 v27, v27
	v_cvt_f32_i32_e32 v28, v28
	v_cvt_f32_i32_e32 v29, v29
	v_cvt_f32_i32_e32 v30, v30
	v_cvt_f32_i32_e32 v31, v31
	v_cvt_f32_i32_e32 v32, v32
	v_cvt_f32_i32_e32 v33, v33
	v_cvt_f32_i32_e32 v34, v34
	v_cvt_f32_i32_e32 v35, v35
	v_cvt_f32_i32_e32 v18, v18
	v_cvt_f32_i32_e32 v19, v19
	v_cvt_f32_i32_e32 v16, v16
	v_cvt_f32_i32_e32 v17, v17
	v_cvt_f32_i32_e32 v14, v14
	v_cvt_f32_i32_e32 v15, v15
	v_cvt_f32_i32_e32 v12, v12
	v_cvt_f32_i32_e32 v13, v13
	v_cvt_f32_i32_e32 v10, v10
	v_cvt_f32_i32_e32 v11, v11
	v_cvt_f32_i32_e32 v8, v8
	v_cvt_f32_i32_e32 v9, v9
	v_cvt_f32_i32_e32 v6, v6
	v_cvt_f32_i32_e32 v7, v7
	v_cvt_f32_i32_e32 v4, v4
	v_cvt_f32_i32_e32 v5, v5
	v_cvt_f32_i32_e32 v131, v131
	v_cvt_f32_i32_e32 v132, v132
	v_cvt_f32_i32_e32 v133, v133
	v_cvt_f32_i32_e32 v134, v134
	v_mul_f32_e32 v131, 0xc3000000, v131
	v_mul_f32_e32 v132, 0xc3000000, v132
	v_mul_f32_e32 v133, 0xc3000000, v133
	v_mul_f32_e32 v134, 0xc3000000, v134
	v_sub_f32_e32 v54, v54, v58
	v_sub_f32_e32 v55, v55, v59
	v_sub_f32_e32 v56, v56, v60
	v_sub_f32_e32 v57, v57, v61
	v_sub_f32_e32 v62, v62, v66
	v_sub_f32_e32 v63, v63, v67
	v_sub_f32_e32 v64, v64, v68
	v_sub_f32_e32 v65, v65, v69
	v_sub_f32_e32 v36, v36, v40
	v_sub_f32_e32 v37, v37, v41
	v_sub_f32_e32 v38, v38, v42
	v_sub_f32_e32 v39, v39, v43
	v_sub_f32_e32 v44, v44, v50
	v_sub_f32_e32 v45, v45, v51
	v_sub_f32_e32 v46, v46, v52
	v_sub_f32_e32 v47, v47, v53
	v_sub_f32_e32 v20, v20, v24
	v_sub_f32_e32 v21, v21, v25
	v_sub_f32_e32 v22, v22, v26
	v_sub_f32_e32 v23, v23, v27
	v_sub_f32_e32 v28, v28, v32
	v_sub_f32_e32 v29, v29, v33
	v_sub_f32_e32 v30, v30, v34
	v_sub_f32_e32 v31, v31, v35
	v_sub_f32_e32 v18, v18, v14
	v_sub_f32_e32 v19, v19, v15
	v_sub_f32_e32 v16, v16, v12
	v_sub_f32_e32 v17, v17, v13
	v_sub_f32_e32 v10, v10, v6
	v_sub_f32_e32 v11, v11, v7
	v_sub_f32_e32 v8, v8, v4
	v_sub_f32_e32 v9, v9, v5
	v_fmamk_f32 v54, v54, 0x41800000, v131
	v_fmamk_f32 v55, v55, 0x41800000, v131
	v_fmamk_f32 v56, v56, 0x41800000, v131
	v_fmamk_f32 v57, v57, 0x41800000, v131
	v_fmamk_f32 v62, v62, 0x41800000, v131
	v_fmamk_f32 v63, v63, 0x41800000, v131
	v_fmamk_f32 v64, v64, 0x41800000, v131
	v_fmamk_f32 v65, v65, 0x41800000, v131
	v_fmamk_f32 v36, v36, 0x41800000, v132
	v_fmamk_f32 v37, v37, 0x41800000, v132
	v_fmamk_f32 v38, v38, 0x41800000, v132
	v_fmamk_f32 v39, v39, 0x41800000, v132
	v_fmamk_f32 v44, v44, 0x41800000, v132
	v_fmamk_f32 v45, v45, 0x41800000, v132
	v_fmamk_f32 v46, v46, 0x41800000, v132
	v_fmamk_f32 v47, v47, 0x41800000, v132
	v_fmamk_f32 v20, v20, 0x41800000, v133
	v_fmamk_f32 v21, v21, 0x41800000, v133
	v_fmamk_f32 v22, v22, 0x41800000, v133
	v_fmamk_f32 v23, v23, 0x41800000, v133
	v_fmamk_f32 v28, v28, 0x41800000, v133
	v_fmamk_f32 v29, v29, 0x41800000, v133
	v_fmamk_f32 v30, v30, 0x41800000, v133
	v_fmamk_f32 v31, v31, 0x41800000, v133
	v_fmamk_f32 v18, v18, 0x41800000, v134
	v_fmamk_f32 v19, v19, 0x41800000, v134
	v_fmamk_f32 v16, v16, 0x41800000, v134
	v_fmamk_f32 v17, v17, 0x41800000, v134
	v_fmamk_f32 v10, v10, 0x41800000, v134
	v_fmamk_f32 v11, v11, 0x41800000, v134
	v_fmamk_f32 v8, v8, 0x41800000, v134
	v_fmamk_f32 v9, v9, 0x41800000, v134
	v_mul_f32_e32 v54, v121, v54
	v_mul_f32_e32 v55, v121, v55
	v_mul_f32_e32 v56, v121, v56
	v_mul_f32_e32 v57, v121, v57
	v_mul_f32_e32 v58, v121, v58
	v_mul_f32_e32 v59, v121, v59
	v_mul_f32_e32 v60, v121, v60
	v_mul_f32_e32 v61, v121, v61
	v_mul_f32_e32 v62, v121, v62
	v_mul_f32_e32 v63, v121, v63
	v_mul_f32_e32 v64, v121, v64
	v_mul_f32_e32 v65, v121, v65
	v_mul_f32_e32 v66, v121, v66
	v_mul_f32_e32 v67, v121, v67
	v_mul_f32_e32 v68, v121, v68
	v_mul_f32_e32 v69, v121, v69
	v_mul_f32_e32 v36, v120, v36
	v_mul_f32_e32 v37, v120, v37
	v_mul_f32_e32 v38, v120, v38
	v_mul_f32_e32 v39, v120, v39
	v_mul_f32_e32 v40, v120, v40
	v_mul_f32_e32 v41, v120, v41
	v_mul_f32_e32 v42, v120, v42
	v_mul_f32_e32 v43, v120, v43
	v_mul_f32_e32 v44, v120, v44
	v_mul_f32_e32 v45, v120, v45
	v_mul_f32_e32 v46, v120, v46
	v_mul_f32_e32 v47, v120, v47
	v_mul_f32_e32 v50, v120, v50
	v_mul_f32_e32 v51, v120, v51
	v_mul_f32_e32 v52, v120, v52
	v_mul_f32_e32 v53, v120, v53
	v_mul_f32_e32 v20, v119, v20
	v_mul_f32_e32 v21, v119, v21
	v_mul_f32_e32 v22, v119, v22
	v_mul_f32_e32 v23, v119, v23
	v_mul_f32_e32 v24, v119, v24
	v_mul_f32_e32 v25, v119, v25
	v_mul_f32_e32 v26, v119, v26
	v_mul_f32_e32 v27, v119, v27
	v_mul_f32_e32 v28, v119, v28
	v_mul_f32_e32 v29, v119, v29
	v_mul_f32_e32 v30, v119, v30
	v_mul_f32_e32 v31, v119, v31
	v_mul_f32_e32 v32, v119, v32
	v_mul_f32_e32 v33, v119, v33
	v_mul_f32_e32 v34, v119, v34
	v_mul_f32_e32 v35, v119, v35
	v_mul_f32_e32 v18, v117, v18
	v_mul_f32_e32 v19, v117, v19
	v_mul_f32_e32 v16, v117, v16
	v_mul_f32_e32 v17, v117, v17
	v_mul_f32_e32 v14, v117, v14
	v_mul_f32_e32 v15, v117, v15
	v_mul_f32_e32 v12, v117, v12
	v_mul_f32_e32 v13, v117, v13
	v_mul_f32_e32 v10, v117, v10
	v_mul_f32_e32 v11, v117, v11
	v_mul_f32_e32 v8, v117, v8
	v_mul_f32_e32 v9, v117, v9
	v_mul_f32_e32 v6, v117, v6
	v_mul_f32_e32 v7, v117, v7
	v_mul_f32_e32 v4, v117, v4
	v_mul_f32_e32 v5, v117, v5
	v_cvt_f32_i32_e32 v0, v108
	v_cvt_f32_i32_e32 v1, v109
	v_cvt_f32_i32_e32 v2, v106
	v_cvt_f32_i32_e32 v3, v107
	v_cvt_f32_i32_e32 v104, v104
	v_cvt_f32_i32_e32 v105, v105
	v_cvt_f32_i32_e32 v102, v102
	v_cvt_f32_i32_e32 v103, v103
	v_cvt_f32_i32_e32 v100, v100
	v_cvt_f32_i32_e32 v101, v101
	v_cvt_f32_i32_e32 v98, v98
	v_cvt_f32_i32_e32 v99, v99
	v_cvt_f32_i32_e32 v96, v96
	v_cvt_f32_i32_e32 v97, v97
	v_cvt_f32_i32_e32 v94, v94
	v_cvt_f32_i32_e32 v95, v95

; #define LAS __attribute__((address_space(3)))
;     ...
;     float wsj[PE_NT];
; #pragma unroll
;     for (int j = 0; j < PE_NT; ++j) {
;         LAS unsigned* lt = lw + j * PE_TOK_W + 128;
;         const float a0 = __builtin_bit_cast(float, lt[2 * lane]), a1 = __builtin_bit_cast(float, lt[2 * lane + 1]);
;         const float wm = fmaxf(wave_max(fmaxf(fabsf(a0), fabsf(a1))), 1e-30f), wq = 127.0f * __builtin_amdgcn_rcpf(wm);
;         wsj[j] = wm * (1.0f / 127.0f);
;         const unsigned pr = (__builtin_bit_cast(unsigned, __builtin_fmaf(a0, wq, 12582912.0f)) & 0xffu) | ((__builtin_bit_cast(unsigned, __builtin_fmaf(a1, wq, 12582912.0f)) & 0xffu) << 8);
;         const unsigned nbp = (unsigned)__builtin_amdgcn_update_dpp(0, (int)pr, 0xB1, 0xF, 0xF, true);
;         asm volatile("" ::: "memory");
;         if ((lane & 1) == 0) lt[2 * lane] = pr | (nbp << 16);
;     }
.LBB0_2861:
	s_waitcnt vmcnt(0)
	s_waitcnt vmcnt(0)
	s_waitcnt vmcnt(0)
	s_waitcnt lgkmcnt(0)
	v_add_u32_e32 v1, s90, v118
	ds_read_b64 v[126:127], v1
	ds_read_b64 v[128:129], v1 offset:1024
	ds_read_b64 v[2:3], v1 offset:512
	s_mov_b32 s0, 0xc0c0500
	v_and_b32_e32 v5, 1, v50
	v_cmp_eq_u32_e32 vcc, 0, v5
	s_waitcnt lgkmcnt(0)
	v_cvt_f32_i32_e32 v126, v126
	v_cvt_f32_i32_e32 v127, v127
	v_mul_f32_e32 v126, v128, v126
	v_mul_f32_e32 v127, v129, v127
	v_mul_f32_e32 v94, v126, v126
	v_mul_f32_e32 v95, v127, v127
	v_fmamk_f32 v94, v94, 0xbdd2d3e8, v113
	v_fmamk_f32 v95, v95, 0xbdd2d3e8, v113
	v_mul_f32_e32 v94, v126, v94
	v_mul_f32_e32 v95, v127, v95
	v_exp_f32_e32 v94, v94
	v_exp_f32_e32 v95, v95
	s_nop 0
	v_add_f32_e32 v94, 1.0, v94
	v_add_f32_e32 v95, 1.0, v95
	v_rcp_f32_e32 v94, v94
	v_rcp_f32_e32 v95, v95
	s_nop 0
	v_mul_f32_e32 v126, v126, v94
	v_mul_f32_e32 v127, v127, v95
	v_mul_f32_e32 v2, v2, v126
	v_mul_f32_e32 v3, v3, v127
	v_max_f32_e64 v0, |v3|, |v3|
	v_max_f32_e64 v4, |v2|, |v2|
	v_max_f32_e32 v0, v4, v0
	s_nop 1
	v_mov_b32_dpp v4, v0 quad_perm:[1,0,3,2] row_mask:0xf bank_mask:0xf bound_ctrl:1
	v_max_f32_e32 v4, v4, v4
	v_max_f32_e32 v0, v0, v4
	s_nop 1
	v_mov_b32_dpp v4, v0 quad_perm:[2,3,0,1] row_mask:0xf bank_mask:0xf bound_ctrl:1
	v_max_f32_e32 v4, v4, v4
	v_max_f32_e32 v0, v0, v4
	s_nop 1
	v_mov_b32_dpp v4, v0 row_half_mirror row_mask:0xf bank_mask:0xf bound_ctrl:1
	v_max_f32_e32 v4, v4, v4
	v_max_f32_e32 v0, v0, v4
	s_nop 1
	v_mov_b32_dpp v4, v0 row_mirror row_mask:0xf bank_mask:0xf bound_ctrl:1
	v_max_f32_e32 v4, v4, v4
	v_max_f32_e32 v0, v0, v4
	v_mov_b32_e32 v4, v0
	s_nop 1
	v_permlane16_swap_b32_e32 v0, v4
	v_max_f32 v0, v0, v4
	s_nop 1
	s_nop 0
	v_mov_b32_e32 v4, v0
	s_nop 1
	v_permlane32_swap_b32_e32 v0, v4
	v_max_f32 v0, v0, v4
	s_nop 0
	v_max_f32_e32 v0, v0, v0
	v_max_f32_e32 v0, 0xda24260, v0
	v_rcp_f32_e32 v4, v0
	s_nop 0
	v_mul_f32_e32 v4, 0x42fe0000, v4
	v_fmaak_f32 v3, v3, v4, 0x4b400000
	v_fmaak_f32 v2, v2, v4, 0x4b400000
	v_lshlrev_b32_e32 v3, 8, v3
	v_perm_b32 v2, v3, v2, s0
	s_nop 1
	v_mov_b32_dpp v3, v2 quad_perm:[1,0,3,2] row_mask:0xf bank_mask:0xf bound_ctrl:1
	s_and_saveexec_b64 s[0:1], vcc
	v_lshl_or_b32 v2, v3, 16, v2
	ds_write_b32 v1, v2 offset:512
	s_or_b64 exec, exec, s[0:1]
	ds_read_b64 v[126:127], v1 offset:1680
	ds_read_b64 v[128:129], v1 offset:2704
	ds_read_b64 v[4:5], v1 offset:2192
	s_mov_b32 s0, 0xc0c0500
	s_waitcnt lgkmcnt(0)
	v_cvt_f32_i32_e32 v126, v126
	v_cvt_f32_i32_e32 v127, v127
	v_mul_f32_e32 v126, v128, v126
	v_mul_f32_e32 v127, v129, v127
	v_mul_f32_e32 v94, v126, v126
	v_mul_f32_e32 v95, v127, v127
	v_fmamk_f32 v94, v94, 0xbdd2d3e8, v113
	v_fmamk_f32 v95, v95, 0xbdd2d3e8, v113
	v_mul_f32_e32 v94, v126, v94
	v_mul_f32_e32 v95, v127, v95
	v_exp_f32_e32 v94, v94
	v_exp_f32_e32 v95, v95
	s_nop 0
	v_add_f32_e32 v94, 1.0, v94
	v_add_f32_e32 v95, 1.0, v95
	v_rcp_f32_e32 v94, v94
	v_rcp_f32_e32 v95, v95
	s_nop 0
	v_mul_f32_e32 v126, v126, v94
	v_mul_f32_e32 v127, v127, v95
	v_mul_f32_e32 v4, v4, v126
	v_mul_f32_e32 v5, v5, v127
	v_max_f32_e64 v2, |v5|, |v5|
	v_max_f32_e64 v3, |v4|, |v4|
	v_max_f32_e32 v2, v3, v2
	s_nop 1
	v_mov_b32_dpp v3, v2 quad_perm:[1,0,3,2] row_mask:0xf bank_mask:0xf bound_ctrl:1
	v_max_f32_e32 v3, v3, v3
	v_max_f32_e32 v2, v2, v3
	s_nop 1
	v_mov_b32_dpp v3, v2 quad_perm:[2,3,0,1] row_mask:0xf bank_mask:0xf bound_ctrl:1
	v_max_f32_e32 v3, v3, v3
	v_max_f32_e32 v2, v2, v3
	s_nop 1
	v_mov_b32_dpp v3, v2 row_half_mirror row_mask:0xf bank_mask:0xf bound_ctrl:1
	v_max_f32_e32 v3, v3, v3
	v_max_f32_e32 v2, v2, v3
	s_nop 1
	v_mov_b32_dpp v3, v2 row_mirror row_mask:0xf bank_mask:0xf bound_ctrl:1
	v_max_f32_e32 v3, v3, v3
	v_max_f32_e32 v2, v2, v3
	v_mov_b32_e32 v3, v2
	s_nop 1
	v_permlane16_swap_b32_e32 v2, v3
	v_max_f32 v2, v2, v3
	s_nop 1
	s_nop 0
	v_mov_b32_e32 v3, v2
	s_nop 1
	v_permlane32_swap_b32_e32 v2, v3
	v_max_f32 v2, v2, v3
	s_nop 0
	v_max_f32_e32 v2, v2, v2
	v_max_f32_e32 v2, 0xda24260, v2
	v_rcp_f32_e32 v3, v2
	s_nop 0
	v_mul_f32_e32 v3, 0x42fe0000, v3
	v_fmaak_f32 v4, v4, v3, 0x4b400000
	v_fmaak_f32 v3, v5, v3, 0x4b400000
	v_lshlrev_b32_e32 v3, 8, v3
	v_perm_b32 v3, v3, v4, s0
	s_nop 1
	v_mov_b32_dpp v4, v3 quad_perm:[1,0,3,2] row_mask:0xf bank_mask:0xf bound_ctrl:1
	s_and_saveexec_b64 s[0:1], vcc
	v_lshl_or_b32 v3, v4, 16, v3
	ds_write_b32 v1, v3 offset:2192
	s_or_b64 exec, exec, s[0:1]
	ds_read_b64 v[126:127], v1 offset:3360
	ds_read_b64 v[128:129], v1 offset:4384
	ds_read_b64 v[4:5], v1 offset:3872
	s_mov_b32 s0, 0xc0c0500
	s_waitcnt lgkmcnt(0)
	v_cvt_f32_i32_e32 v126, v126
	v_cvt_f32_i32_e32 v127, v127
	v_mul_f32_e32 v126, v128, v126
	v_mul_f32_e32 v127, v129, v127
	v_mul_f32_e32 v94, v126, v126
	v_mul_f32_e32 v95, v127, v127
	v_fmamk_f32 v94, v94, 0xbdd2d3e8, v113
	v_fmamk_f32 v95, v95, 0xbdd2d3e8, v113
	v_mul_f32_e32 v94, v126, v94
	v_mul_f32_e32 v95, v127, v95
	v_exp_f32_e32 v94, v94
	v_exp_f32_e32 v95, v95
	s_nop 0
	v_add_f32_e32 v94, 1.0, v94
	v_add_f32_e32 v95, 1.0, v95
	v_rcp_f32_e32 v94, v94
	v_rcp_f32_e32 v95, v95
	s_nop 0
	v_mul_f32_e32 v126, v126, v94
	v_mul_f32_e32 v127, v127, v95
	v_mul_f32_e32 v4, v4, v126
	v_mul_f32_e32 v5, v5, v127
	v_max_f32_e64 v3, |v5|, |v5|
	v_max_f32_e64 v6, |v4|, |v4|
	v_max_f32_e32 v3, v6, v3
	s_nop 1
	v_mov_b32_dpp v6, v3 quad_perm:[1,0,3,2] row_mask:0xf bank_mask:0xf bound_ctrl:1
	v_max_f32_e32 v6, v6, v6
	v_max_f32_e32 v3, v3, v6
	s_nop 1
	v_mov_b32_dpp v6, v3 quad_perm:[2,3,0,1] row_mask:0xf bank_mask:0xf bound_ctrl:1
	v_max_f32_e32 v6, v6, v6
	v_max_f32_e32 v3, v3, v6
	s_nop 1
	v_mov_b32_dpp v6, v3 row_half_mirror row_mask:0xf bank_mask:0xf bound_ctrl:1
	v_max_f32_e32 v6, v6, v6
	v_max_f32_e32 v3, v3, v6
	s_nop 1
	v_mov_b32_dpp v6, v3 row_mirror row_mask:0xf bank_mask:0xf bound_ctrl:1
	v_max_f32_e32 v6, v6, v6
	v_max_f32_e32 v3, v3, v6
	v_mov_b32_e32 v6, v3
	s_nop 1
	v_permlane16_swap_b32_e32 v3, v6
	v_max_f32 v3, v3, v6
	s_nop 1
	s_nop 0
	v_mov_b32_e32 v6, v3
	s_nop 1
	v_permlane32_swap_b32_e32 v3, v6
	v_max_f32 v3, v3, v6
	s_nop 0
	v_max_f32_e32 v3, v3, v3
	v_max_f32_e32 v3, 0xda24260, v3
	v_rcp_f32_e32 v6, v3
	s_nop 0
	v_mul_f32_e32 v6, 0x42fe0000, v6
	v_fmaak_f32 v5, v5, v6, 0x4b400000
	v_fmaak_f32 v4, v4, v6, 0x4b400000
	v_lshlrev_b32_e32 v5, 8, v5
	v_perm_b32 v4, v5, v4, s0
	s_nop 1
	v_mov_b32_dpp v5, v4 quad_perm:[1,0,3,2] row_mask:0xf bank_mask:0xf bound_ctrl:1
	s_and_saveexec_b64 s[0:1], vcc
	v_lshl_or_b32 v4, v5, 16, v4
	ds_write_b32 v1, v4 offset:3872
	s_or_b64 exec, exec, s[0:1]
	ds_read_b64 v[126:127], v1 offset:5040
	ds_read_b64 v[128:129], v1 offset:6064
	ds_read_b64 v[6:7], v1 offset:5552
	s_mov_b32 s0, 0xc0c0500
	s_waitcnt lgkmcnt(0)
; #define LAS __attribute__((address_space(3)))
; #define LDS_WAIT() asm volatile("s_waitcnt lgkmcnt(0)" ::: "memory")
;     ...
;     float wsj[PE_NT];
; #pragma unroll
;     for (int j = 0; j < PE_NT; ++j) {
;         LAS unsigned* lt = lw + j * PE_TOK_W + 128;
;         const float a0 = __builtin_bit_cast(float, lt[2 * lane]), a1 = __builtin_bit_cast(float, lt[2 * lane + 1]);
;         const float wm = fmaxf(wave_max(fmaxf(fabsf(a0), fabsf(a1))), 1e-30f), wq = 127.0f * __builtin_amdgcn_rcpf(wm);
;         wsj[j] = wm * (1.0f / 127.0f);
;         const unsigned pr = (__builtin_bit_cast(unsigned, __builtin_fmaf(a0, wq, 12582912.0f)) & 0xffu) | ((__builtin_bit_cast(unsigned, __builtin_fmaf(a1, wq, 12582912.0f)) & 0xffu) << 8);
;         const unsigned nbp = (unsigned)__builtin_amdgcn_update_dpp(0, (int)pr, 0xB1, 0xF, 0xF, true);
;         asm volatile("" ::: "memory");
;         if ((lane & 1) == 0) lt[2 * lane] = pr | (nbp << 16);
;     }
;     LDS_WAIT(); asm volatile("" ::: "memory");
;     {
;         unsigned er[PE_RD];
; #pragma unroll
;         for (int q = 0; q < PE_RD; ++q) { const v4u rec = *(const LAS v4u*)(ents + 4 * q); er[q] = __builtin_amdgcn_readfirstlane(rec.x); PE_ISSUE4(q, rec, VB8); }
;         int curi[16];
; #pragma unroll
;         for (int i = 0; i < 16; ++i) curi[i] = 0;
;         int jcur = (int)((er[0] >> 14) & 3u);
;         v4u nrec = *(const LAS v4u*)(ents + 4 * PE_RD);
	v_cvt_f32_i32_e32 v126, v126
	v_cvt_f32_i32_e32 v127, v127
	v_mul_f32_e32 v126, v128, v126
	v_mul_f32_e32 v127, v129, v127
	v_mul_f32_e32 v94, v126, v126
	v_mul_f32_e32 v95, v127, v127
	v_fmamk_f32 v94, v94, 0xbdd2d3e8, v113
	v_fmamk_f32 v95, v95, 0xbdd2d3e8, v113
	v_mul_f32_e32 v94, v126, v94
	v_mul_f32_e32 v95, v127, v95
	v_exp_f32_e32 v94, v94
	v_exp_f32_e32 v95, v95
	s_nop 0
	v_add_f32_e32 v94, 1.0, v94
	v_add_f32_e32 v95, 1.0, v95
	v_rcp_f32_e32 v94, v94
	v_rcp_f32_e32 v95, v95
	s_nop 0
	v_mul_f32_e32 v126, v126, v94
	v_mul_f32_e32 v127, v127, v95
	v_mul_f32_e32 v6, v6, v126
	v_mul_f32_e32 v7, v7, v127
	v_max_f32_e64 v4, |v7|, |v7|
	v_max_f32_e64 v5, |v6|, |v6|
	v_max_f32_e32 v4, v5, v4
	s_nop 1
	v_mov_b32_dpp v5, v4 quad_perm:[1,0,3,2] row_mask:0xf bank_mask:0xf bound_ctrl:1
	v_max_f32_e32 v5, v5, v5
	v_max_f32_e32 v4, v4, v5
	s_nop 1
	v_mov_b32_dpp v5, v4 quad_perm:[2,3,0,1] row_mask:0xf bank_mask:0xf bound_ctrl:1
	v_max_f32_e32 v5, v5, v5
	v_max_f32_e32 v4, v4, v5
	s_nop 1
	v_mov_b32_dpp v5, v4 row_half_mirror row_mask:0xf bank_mask:0xf bound_ctrl:1
	v_max_f32_e32 v5, v5, v5
	v_max_f32_e32 v4, v4, v5
	s_nop 1
	v_mov_b32_dpp v5, v4 row_mirror row_mask:0xf bank_mask:0xf bound_ctrl:1
	v_max_f32_e32 v5, v5, v5
	v_max_f32_e32 v4, v4, v5
	v_mov_b32_e32 v5, v4
	s_nop 1
	v_permlane16_swap_b32_e32 v4, v5
	v_max_f32 v4, v4, v5
	s_nop 1
	s_nop 0
	v_mov_b32_e32 v5, v4
	s_nop 1
	v_permlane32_swap_b32_e32 v4, v5
	v_max_f32 v4, v4, v5
	s_nop 0
	v_max_f32_e32 v4, v4, v4
	v_max_f32_e32 v4, 0xda24260, v4
	v_rcp_f32_e32 v5, v4
	s_nop 0
	v_mul_f32_e32 v5, 0x42fe0000, v5
	v_fmaak_f32 v6, v6, v5, 0x4b400000
	v_fmaak_f32 v5, v7, v5, 0x4b400000
	v_lshlrev_b32_e32 v5, 8, v5
	v_perm_b32 v5, v5, v6, s0
	s_nop 1
	v_mov_b32_dpp v6, v5 quad_perm:[1,0,3,2] row_mask:0xf bank_mask:0xf bound_ctrl:1
	s_and_saveexec_b64 s[0:1], vcc
	v_lshl_or_b32 v5, v6, 16, v5
	ds_write_b32 v1, v5 offset:5552
	s_or_b64 exec, exec, s[0:1]
	s_waitcnt lgkmcnt(0)
	v_mov_b32_e32 v1, s90
	ds_read_b128 v[6:9], v1 offset:6720
	v_mul_f32_e32 v119, 0x3c010204, v3
	v_mul_f32_e32 v117, 0x3c010204, v4
	v_mul_f32_e32 v121, 0x3c010204, v0
	v_mul_f32_e32 v120, 0x3c010204, v2
	s_waitcnt lgkmcnt(0)
	v_lshlrev_b32_e32 v5, 9, v6
	v_and_b32_e32 v5, 0x7ffe00, v5
	v_add_u32_e32 v5, v5, v118
	global_load_dwordx2 v[70:71], v5, s[82:83]
	v_lshl_add_u32 v7, v7, 9, v118
	global_load_dwordx2 v[72:73], v7, s[82:83]
	v_lshl_add_u32 v8, v8, 9, v118
	global_load_dwordx2 v[74:75], v8, s[82:83]
	v_lshl_add_u32 v9, v9, 9, v118
	global_load_dwordx2 v[80:81], v9, s[82:83]
	ds_read_b128 v[8:11], v1 offset:6736
	v_readfirstlane_b32 s4, v6
	s_bfe_u32 s7, s4, 0x2000e
	s_andn2_b64 vcc, exec, s[2:3]
	s_mov_b32 s0, 0
	s_waitcnt lgkmcnt(0)
	v_lshlrev_b32_e32 v3, 9, v8
	v_and_b32_e32 v3, 0x7ffe00, v3
	v_add_u32_e32 v3, v3, v118
	global_load_dwordx2 v[76:77], v3, s[82:83]
	v_lshl_add_u32 v4, v9, 9, v118
	global_load_dwordx2 v[82:83], v4, s[82:83]
	v_lshl_add_u32 v5, v10, 9, v118
	global_load_dwordx2 v[84:85], v5, s[82:83]
	v_lshl_add_u32 v3, v11, 9, v118
	global_load_dwordx2 v[90:91], v3, s[82:83]
	ds_read_b128 v[10:13], v1 offset:6752
	v_readfirstlane_b32 s5, v8
	s_waitcnt lgkmcnt(0)
	v_lshlrev_b32_e32 v0, 9, v10
	v_and_b32_e32 v0, 0x7ffe00, v0
	v_add_u32_e32 v0, v0, v118
	global_load_dwordx2 v[78:79], v0, s[82:83]
	v_lshl_add_u32 v0, v11, 9, v118
	global_load_dwordx2 v[86:87], v0, s[82:83]
	v_lshl_add_u32 v0, v12, 9, v118
	global_load_dwordx2 v[88:89], v0, s[82:83]
	v_lshl_add_u32 v0, v13, 9, v118
	global_load_dwordx2 v[92:93], v0, s[82:83]
	v_readfirstlane_b32 s8, v10
	s_cbranch_vccnz .LBB0_2884
	v_mov_b32_e32 v48, v49
	v_mov_b32_e32 v130, 0x1010101
	v_mov_b32_e32 v131, 0
	v_mov_b32_e32 v132, 0
	v_mov_b32_e32 v133, 0
	v_mov_b32_e32 v134, 0
	v_mov_b32_e32 v94, 0
	v_mov_b32_e32 v95, 0
	v_mov_b32_e32 v96, 0
	v_mov_b32_e32 v97, 0
	v_mov_b32_e32 v98, 0
	v_mov_b32_e32 v99, 0
	v_mov_b32_e32 v100, 0
	v_mov_b32_e32 v101, 0
	v_mov_b32_e32 v102, 0
	v_mov_b32_e32 v103, 0
	v_mov_b32_e32 v104, 0
	v_mov_b32_e32 v105, 0
	v_mov_b32_e32 v106, 0
	v_mov_b32_e32 v107, 0
	v_mov_b32_e32 v108, 0
	v_mov_b32_e32 v109, 0
	v_readlane_b32 s1, v255, 2
	v_mov_b64_e32 v[12:13], v[48:49]
	v_mov_b64_e32 v[14:15], v[48:49]
	v_mov_b64_e32 v[16:17], v[48:49]
	v_mov_b64_e32 v[18:19], v[48:49]
	v_mov_b64_e32 v[34:35], v[48:49]
	v_mov_b64_e32 v[32:33], v[48:49]
	v_mov_b64_e32 v[30:31], v[48:49]
	v_mov_b64_e32 v[28:29], v[48:49]
	v_mov_b64_e32 v[26:27], v[48:49]
	v_mov_b64_e32 v[24:25], v[48:49]
	v_mov_b64_e32 v[22:23], v[48:49]
	v_mov_b64_e32 v[20:21], v[48:49]
	v_mov_b64_e32 v[52:53], v[48:49]
	v_mov_b64_e32 v[50:51], v[48:49]
	v_mov_b64_e32 v[46:47], v[48:49]
	v_mov_b64_e32 v[44:45], v[48:49]
	v_mov_b64_e32 v[42:43], v[48:49]
	v_mov_b64_e32 v[40:41], v[48:49]
	v_mov_b64_e32 v[38:39], v[48:49]
	v_mov_b64_e32 v[36:37], v[48:49]
	v_mov_b64_e32 v[68:69], v[48:49]
	v_mov_b64_e32 v[66:67], v[48:49]
	v_mov_b64_e32 v[64:65], v[48:49]
	v_mov_b64_e32 v[62:63], v[48:49]
	v_mov_b64_e32 v[60:61], v[48:49]
	v_mov_b64_e32 v[58:59], v[48:49]
	v_mov_b64_e32 v[56:57], v[48:49]
	v_mov_b64_e32 v[54:55], v[48:49]
	v_mov_b64_e32 v[10:11], v[48:49]
	v_mov_b64_e32 v[8:9], v[48:49]
	v_mov_b64_e32 v[6:7], v[48:49]
	v_mov_b64_e32 v[4:5], v[48:49]
	s_branch .LBB0_2873
.LvC_t0:
	s_mulk_i32 s2, 0x690
	s_lshr_b32 s3, s8, 17
	s_add_i32 s2, s90, s2
	s_and_b32 s3, s3, 0x7ffc
	s_add_i32 s2, s2, s3
	v_mov_b32_e32 v48, s2
	ds_read_b32 v48, v48 offset:512
	v_perm_b32 v126, v86, v78, s91
	v_perm_b32 v78, v86, v78, s92
	v_perm_b32 v86, v92, v88, s91
	v_perm_b32 v88, v92, v88, s92
	v_perm_b32 v92, v86, v126, s94
	v_perm_b32 v86, v86, v126, s68
	v_perm_b32 v126, v88, v78, s94
	v_perm_b32 v78, v88, v78, s68
	s_waitcnt lgkmcnt(0)
	v_dot4_i32_i8 v54, v92, v48, v54
	v_dot4_i32_i8 v55, v86, v48, v55
	v_dot4_i32_i8 v56, v126, v48, v56
	v_dot4_i32_i8 v57, v78, v48, v57
	v_and_b32_e32 v86, 0xf0f0f0f0, v86
	v_and_b32_e32 v78, 0xf0f0f0f0, v78
	v_and_b32_e32 v88, 0xf0f0f0f0, v92
	v_and_b32_e32 v92, 0xf0f0f0f0, v126
	v_dot4_i32_i8 v58, v88, v48, v58
	v_dot4_i32_i8 v59, v86, v48, v59
	v_dot4_i32_i8 v60, v92, v48, v60
	v_dot4_i32_i8 v61, v78, v48, v61
	v_perm_b32 v78, v87, v79, s91
	v_perm_b32 v86, v93, v89, s91
	v_perm_b32 v79, v87, v79, s92
	v_perm_b32 v87, v93, v89, s92
	v_perm_b32 v88, v86, v78, s94
	v_perm_b32 v78, v86, v78, s68
	v_perm_b32 v86, v87, v79, s94
	v_perm_b32 v79, v87, v79, s68
	v_dot4_i32_i8 v62, v88, v48, v62
	v_dot4_i32_i8 v63, v78, v48, v63
	v_dot4_i32_i8 v64, v86, v48, v64
	v_dot4_i32_i8 v65, v79, v48, v65
	v_and_b32_e32 v87, 0xf0f0f0f0, v88
	v_and_b32_e32 v78, 0xf0f0f0f0, v78
	v_and_b32_e32 v86, 0xf0f0f0f0, v86
	v_and_b32_e32 v79, 0xf0f0f0f0, v79
	v_dot4_i32_i8 v66, v87, v48, v66
	v_dot4_i32_i8 v67, v78, v48, v67
	v_dot4_i32_i8 v68, v86, v48, v68
	v_dot4_i32_i8 v69, v79, v48, v69
	v_dot4_i32_i8 v131, v130, v48, v131
	s_branch .LBB0_2872
.LvC_t1:
	s_mulk_i32 s2, 0x690
	s_lshr_b32 s3, s8, 17
	s_add_i32 s2, s90, s2
	s_and_b32 s3, s3, 0x7ffc
	s_add_i32 s2, s2, s3
	v_mov_b32_e32 v48, s2
	ds_read_b32 v48, v48 offset:512
	v_perm_b32 v126, v86, v78, s91
	v_perm_b32 v78, v86, v78, s92
	v_perm_b32 v86, v92, v88, s91
	v_perm_b32 v88, v92, v88, s92
	v_perm_b32 v92, v86, v126, s94
	v_perm_b32 v86, v86, v126, s68
	v_perm_b32 v126, v88, v78, s94
	v_perm_b32 v78, v88, v78, s68
	s_waitcnt lgkmcnt(0)
	v_dot4_i32_i8 v36, v92, v48, v36
	v_dot4_i32_i8 v37, v86, v48, v37
	v_dot4_i32_i8 v38, v126, v48, v38
	v_dot4_i32_i8 v39, v78, v48, v39
	v_and_b32_e32 v86, 0xf0f0f0f0, v86
	v_and_b32_e32 v78, 0xf0f0f0f0, v78
	v_and_b32_e32 v88, 0xf0f0f0f0, v92
	v_and_b32_e32 v92, 0xf0f0f0f0, v126
	v_dot4_i32_i8 v40, v88, v48, v40
	v_dot4_i32_i8 v41, v86, v48, v41
	v_dot4_i32_i8 v42, v92, v48, v42
	v_dot4_i32_i8 v43, v78, v48, v43
	v_perm_b32 v78, v87, v79, s91
	v_perm_b32 v86, v93, v89, s91
	v_perm_b32 v79, v87, v79, s92
	v_perm_b32 v87, v93, v89, s92
	v_perm_b32 v88, v86, v78, s94
	v_perm_b32 v78, v86, v78, s68
	v_perm_b32 v86, v87, v79, s94
	v_perm_b32 v79, v87, v79, s68
	v_dot4_i32_i8 v44, v88, v48, v44
	v_dot4_i32_i8 v45, v78, v48, v45
	v_dot4_i32_i8 v46, v86, v48, v46
	v_dot4_i32_i8 v47, v79, v48, v47
	v_and_b32_e32 v87, 0xf0f0f0f0, v88
	v_and_b32_e32 v78, 0xf0f0f0f0, v78
	v_and_b32_e32 v86, 0xf0f0f0f0, v86
	v_and_b32_e32 v79, 0xf0f0f0f0, v79
	v_dot4_i32_i8 v50, v87, v48, v50
	v_dot4_i32_i8 v51, v78, v48, v51
	v_dot4_i32_i8 v52, v86, v48, v52
	v_dot4_i32_i8 v53, v79, v48, v53
	v_dot4_i32_i8 v132, v130, v48, v132
	s_branch .LBB0_2872
.LvC_t2:
	s_mulk_i32 s2, 0x690
	s_lshr_b32 s3, s8, 17
	s_add_i32 s2, s90, s2
	s_and_b32 s3, s3, 0x7ffc
	s_add_i32 s2, s2, s3
	v_mov_b32_e32 v48, s2
	ds_read_b32 v48, v48 offset:512
	v_perm_b32 v126, v86, v78, s91
	v_perm_b32 v78, v86, v78, s92
	v_perm_b32 v86, v92, v88, s91
	v_perm_b32 v88, v92, v88, s92
	v_perm_b32 v92, v86, v126, s94
	v_perm_b32 v86, v86, v126, s68
	v_perm_b32 v126, v88, v78, s94
	v_perm_b32 v78, v88, v78, s68
	s_waitcnt lgkmcnt(0)
	v_dot4_i32_i8 v20, v92, v48, v20
	v_dot4_i32_i8 v21, v86, v48, v21
	v_dot4_i32_i8 v22, v126, v48, v22
	v_dot4_i32_i8 v23, v78, v48, v23
	v_and_b32_e32 v86, 0xf0f0f0f0, v86
	v_and_b32_e32 v78, 0xf0f0f0f0, v78
	v_and_b32_e32 v88, 0xf0f0f0f0, v92
	v_and_b32_e32 v92, 0xf0f0f0f0, v126
	v_dot4_i32_i8 v24, v88, v48, v24
	v_dot4_i32_i8 v25, v86, v48, v25
	v_dot4_i32_i8 v26, v92, v48, v26
	v_dot4_i32_i8 v27, v78, v48, v27
	v_perm_b32 v78, v87, v79, s91
	v_perm_b32 v86, v93, v89, s91
	v_perm_b32 v79, v87, v79, s92
	v_perm_b32 v87, v93, v89, s92
	v_perm_b32 v88, v86, v78, s94
	v_perm_b32 v78, v86, v78, s68
	v_perm_b32 v86, v87, v79, s94
	v_perm_b32 v79, v87, v79, s68
	v_dot4_i32_i8 v28, v88, v48, v28
	v_dot4_i32_i8 v29, v78, v48, v29
	v_dot4_i32_i8 v30, v86, v48, v30
	v_dot4_i32_i8 v31, v79, v48, v31
	v_and_b32_e32 v87, 0xf0f0f0f0, v88
	v_and_b32_e32 v78, 0xf0f0f0f0, v78
	v_and_b32_e32 v86, 0xf0f0f0f0, v86
	v_and_b32_e32 v79, 0xf0f0f0f0, v79
	v_dot4_i32_i8 v32, v87, v48, v32
	v_dot4_i32_i8 v33, v78, v48, v33
	v_dot4_i32_i8 v34, v86, v48, v34
	v_dot4_i32_i8 v35, v79, v48, v35
	v_dot4_i32_i8 v133, v130, v48, v133
	s_branch .LBB0_2872
.LvC_t3:
	s_mulk_i32 s2, 0x690
	s_lshr_b32 s3, s8, 17
	s_add_i32 s2, s90, s2
	s_and_b32 s3, s3, 0x7ffc
	s_add_i32 s2, s2, s3
	v_mov_b32_e32 v48, s2
	ds_read_b32 v48, v48 offset:512
	v_perm_b32 v126, v86, v78, s91
	v_perm_b32 v78, v86, v78, s92
	v_perm_b32 v86, v92, v88, s91
	v_perm_b32 v88, v92, v88, s92
	v_perm_b32 v92, v86, v126, s94
	v_perm_b32 v86, v86, v126, s68
	v_perm_b32 v126, v88, v78, s94
	v_perm_b32 v78, v88, v78, s68
	s_waitcnt lgkmcnt(0)
	v_dot4_i32_i8 v18, v92, v48, v18
	v_dot4_i32_i8 v19, v86, v48, v19
	v_dot4_i32_i8 v16, v126, v48, v16
	v_dot4_i32_i8 v17, v78, v48, v17
	v_and_b32_e32 v86, 0xf0f0f0f0, v86
	v_and_b32_e32 v78, 0xf0f0f0f0, v78
	v_and_b32_e32 v88, 0xf0f0f0f0, v92
	v_and_b32_e32 v92, 0xf0f0f0f0, v126
	v_dot4_i32_i8 v14, v88, v48, v14
	v_dot4_i32_i8 v15, v86, v48, v15
	v_dot4_i32_i8 v12, v92, v48, v12
	v_dot4_i32_i8 v13, v78, v48, v13
	v_perm_b32 v78, v87, v79, s91
	v_perm_b32 v86, v93, v89, s91
	v_perm_b32 v79, v87, v79, s92
	v_perm_b32 v87, v93, v89, s92
	v_perm_b32 v88, v86, v78, s94
	v_perm_b32 v78, v86, v78, s68
	v_perm_b32 v86, v87, v79, s94
	v_perm_b32 v79, v87, v79, s68
	v_dot4_i32_i8 v10, v88, v48, v10
	v_dot4_i32_i8 v11, v78, v48, v11
	v_dot4_i32_i8 v8, v86, v48, v8
	v_dot4_i32_i8 v9, v79, v48, v9
	v_and_b32_e32 v87, 0xf0f0f0f0, v88
	v_and_b32_e32 v78, 0xf0f0f0f0, v78
	v_and_b32_e32 v86, 0xf0f0f0f0, v86
	v_and_b32_e32 v79, 0xf0f0f0f0, v79
	v_dot4_i32_i8 v6, v87, v48, v6
	v_dot4_i32_i8 v7, v78, v48, v7
	v_dot4_i32_i8 v4, v86, v48, v4
	v_dot4_i32_i8 v5, v79, v48, v5
	v_dot4_i32_i8 v134, v130, v48, v134

.LvA_t0:
	s_mulk_i32 s2, 0x690
	s_lshr_b32 s3, s4, 17
	s_add_i32 s2, s90, s2
	s_and_b32 s3, s3, 0x7ffc
	s_add_i32 s2, s2, s3
	v_mov_b32_e32 v48, s2
	ds_read_b32 v48, v48 offset:512
	v_perm_b32 v126, v72, v70, s91
	v_perm_b32 v70, v72, v70, s92
	v_perm_b32 v72, v80, v74, s91
	v_perm_b32 v74, v80, v74, s92
	v_perm_b32 v80, v72, v126, s94
	v_perm_b32 v72, v72, v126, s68
	v_perm_b32 v126, v74, v70, s94
	v_perm_b32 v70, v74, v70, s68
	s_waitcnt lgkmcnt(0)
	v_dot4_i32_i8 v54, v80, v48, v54
	v_dot4_i32_i8 v55, v72, v48, v55
	v_dot4_i32_i8 v56, v126, v48, v56
	v_dot4_i32_i8 v57, v70, v48, v57
	v_and_b32_e32 v72, 0xf0f0f0f0, v72
	v_and_b32_e32 v70, 0xf0f0f0f0, v70
	v_and_b32_e32 v74, 0xf0f0f0f0, v80
	v_and_b32_e32 v80, 0xf0f0f0f0, v126
	v_dot4_i32_i8 v58, v74, v48, v58
	v_dot4_i32_i8 v59, v72, v48, v59
	v_dot4_i32_i8 v60, v80, v48, v60
	v_dot4_i32_i8 v61, v70, v48, v61
	v_perm_b32 v70, v73, v71, s91
	v_perm_b32 v72, v81, v75, s91
	v_perm_b32 v71, v73, v71, s92
	v_perm_b32 v73, v81, v75, s92
	v_perm_b32 v74, v72, v70, s94
	v_perm_b32 v70, v72, v70, s68
	v_perm_b32 v72, v73, v71, s94
	v_perm_b32 v71, v73, v71, s68
	v_dot4_i32_i8 v62, v74, v48, v62
	v_dot4_i32_i8 v63, v70, v48, v63
	v_dot4_i32_i8 v64, v72, v48, v64
	v_dot4_i32_i8 v65, v71, v48, v65
	v_and_b32_e32 v73, 0xf0f0f0f0, v74
	v_and_b32_e32 v70, 0xf0f0f0f0, v70
	v_and_b32_e32 v72, 0xf0f0f0f0, v72
	v_and_b32_e32 v71, 0xf0f0f0f0, v71
	v_dot4_i32_i8 v66, v73, v48, v66
	v_dot4_i32_i8 v67, v70, v48, v67
	v_dot4_i32_i8 v68, v72, v48, v68
	v_dot4_i32_i8 v69, v71, v48, v69
	v_dot4_i32_i8 v131, v130, v48, v131
	s_branch .LBB0_2877
.LvA_t1:
	s_mulk_i32 s2, 0x690
	s_lshr_b32 s3, s4, 17
	s_add_i32 s2, s90, s2
	s_and_b32 s3, s3, 0x7ffc
	s_add_i32 s2, s2, s3
	v_mov_b32_e32 v48, s2
	ds_read_b32 v48, v48 offset:512
	v_perm_b32 v126, v72, v70, s91
	v_perm_b32 v70, v72, v70, s92
	v_perm_b32 v72, v80, v74, s91
	v_perm_b32 v74, v80, v74, s92
	v_perm_b32 v80, v72, v126, s94
	v_perm_b32 v72, v72, v126, s68
	v_perm_b32 v126, v74, v70, s94
	v_perm_b32 v70, v74, v70, s68
	s_waitcnt lgkmcnt(0)
	v_dot4_i32_i8 v36, v80, v48, v36
	v_dot4_i32_i8 v37, v72, v48, v37
	v_dot4_i32_i8 v38, v126, v48, v38
	v_dot4_i32_i8 v39, v70, v48, v39
	v_and_b32_e32 v72, 0xf0f0f0f0, v72
	v_and_b32_e32 v70, 0xf0f0f0f0, v70
	v_and_b32_e32 v74, 0xf0f0f0f0, v80
	v_and_b32_e32 v80, 0xf0f0f0f0, v126
	v_dot4_i32_i8 v40, v74, v48, v40
	v_dot4_i32_i8 v41, v72, v48, v41
	v_dot4_i32_i8 v42, v80, v48, v42
	v_dot4_i32_i8 v43, v70, v48, v43
	v_perm_b32 v70, v73, v71, s91
	v_perm_b32 v72, v81, v75, s91
	v_perm_b32 v71, v73, v71, s92
	v_perm_b32 v73, v81, v75, s92
	v_perm_b32 v74, v72, v70, s94
	v_perm_b32 v70, v72, v70, s68
	v_perm_b32 v72, v73, v71, s94
	v_perm_b32 v71, v73, v71, s68
	v_dot4_i32_i8 v44, v74, v48, v44
	v_dot4_i32_i8 v45, v70, v48, v45
	v_dot4_i32_i8 v46, v72, v48, v46
	v_dot4_i32_i8 v47, v71, v48, v47
	v_and_b32_e32 v73, 0xf0f0f0f0, v74
	v_and_b32_e32 v70, 0xf0f0f0f0, v70
	v_and_b32_e32 v72, 0xf0f0f0f0, v72
	v_and_b32_e32 v71, 0xf0f0f0f0, v71
	v_dot4_i32_i8 v50, v73, v48, v50
	v_dot4_i32_i8 v51, v70, v48, v51
	v_dot4_i32_i8 v52, v72, v48, v52
	v_dot4_i32_i8 v53, v71, v48, v53
	v_dot4_i32_i8 v132, v130, v48, v132
	s_branch .LBB0_2877
.LvA_t2:
	s_mulk_i32 s2, 0x690
	s_lshr_b32 s3, s4, 17
	s_add_i32 s2, s90, s2
	s_and_b32 s3, s3, 0x7ffc
	s_add_i32 s2, s2, s3
	v_mov_b32_e32 v48, s2
	ds_read_b32 v48, v48 offset:512
	v_perm_b32 v126, v72, v70, s91
	v_perm_b32 v70, v72, v70, s92
	v_perm_b32 v72, v80, v74, s91
	v_perm_b32 v74, v80, v74, s92
	v_perm_b32 v80, v72, v126, s94
	v_perm_b32 v72, v72, v126, s68
	v_perm_b32 v126, v74, v70, s94
	v_perm_b32 v70, v74, v70, s68
	s_waitcnt lgkmcnt(0)
	v_dot4_i32_i8 v20, v80, v48, v20
	v_dot4_i32_i8 v21, v72, v48, v21
	v_dot4_i32_i8 v22, v126, v48, v22
	v_dot4_i32_i8 v23, v70, v48, v23
	v_and_b32_e32 v72, 0xf0f0f0f0, v72
	v_and_b32_e32 v70, 0xf0f0f0f0, v70
	v_and_b32_e32 v74, 0xf0f0f0f0, v80
	v_and_b32_e32 v80, 0xf0f0f0f0, v126
	v_dot4_i32_i8 v24, v74, v48, v24
	v_dot4_i32_i8 v25, v72, v48, v25
	v_dot4_i32_i8 v26, v80, v48, v26
	v_dot4_i32_i8 v27, v70, v48, v27
	v_perm_b32 v70, v73, v71, s91
	v_perm_b32 v72, v81, v75, s91
	v_perm_b32 v71, v73, v71, s92
	v_perm_b32 v73, v81, v75, s92
	v_perm_b32 v74, v72, v70, s94
	v_perm_b32 v70, v72, v70, s68
	v_perm_b32 v72, v73, v71, s94
	v_perm_b32 v71, v73, v71, s68
	v_dot4_i32_i8 v28, v74, v48, v28
	v_dot4_i32_i8 v29, v70, v48, v29
	v_dot4_i32_i8 v30, v72, v48, v30
	v_dot4_i32_i8 v31, v71, v48, v31
	v_and_b32_e32 v73, 0xf0f0f0f0, v74
	v_and_b32_e32 v70, 0xf0f0f0f0, v70
	v_and_b32_e32 v72, 0xf0f0f0f0, v72
	v_and_b32_e32 v71, 0xf0f0f0f0, v71
	v_dot4_i32_i8 v32, v73, v48, v32
	v_dot4_i32_i8 v33, v70, v48, v33
	v_dot4_i32_i8 v34, v72, v48, v34
	v_dot4_i32_i8 v35, v71, v48, v35
	v_dot4_i32_i8 v133, v130, v48, v133
	s_branch .LBB0_2877
.LvA_t3:
	s_mulk_i32 s2, 0x690
	s_lshr_b32 s3, s4, 17
	s_add_i32 s2, s90, s2
	s_and_b32 s3, s3, 0x7ffc
	s_add_i32 s2, s2, s3
	v_mov_b32_e32 v48, s2
	ds_read_b32 v48, v48 offset:512
	v_perm_b32 v126, v72, v70, s91
	v_perm_b32 v70, v72, v70, s92
	v_perm_b32 v72, v80, v74, s91
	v_perm_b32 v74, v80, v74, s92
	v_perm_b32 v80, v72, v126, s94
	v_perm_b32 v72, v72, v126, s68
	v_perm_b32 v126, v74, v70, s94
	v_perm_b32 v70, v74, v70, s68
	s_waitcnt lgkmcnt(0)
	v_dot4_i32_i8 v18, v80, v48, v18
	v_dot4_i32_i8 v19, v72, v48, v19
	v_dot4_i32_i8 v16, v126, v48, v16
	v_dot4_i32_i8 v17, v70, v48, v17
	v_and_b32_e32 v72, 0xf0f0f0f0, v72
	v_and_b32_e32 v70, 0xf0f0f0f0, v70
	v_and_b32_e32 v74, 0xf0f0f0f0, v80
	v_and_b32_e32 v80, 0xf0f0f0f0, v126
	v_dot4_i32_i8 v14, v74, v48, v14
	v_dot4_i32_i8 v15, v72, v48, v15
	v_dot4_i32_i8 v12, v80, v48, v12
	v_dot4_i32_i8 v13, v70, v48, v13
	v_perm_b32 v70, v73, v71, s91
	v_perm_b32 v72, v81, v75, s91
	v_perm_b32 v71, v73, v71, s92
	v_perm_b32 v73, v81, v75, s92
	v_perm_b32 v74, v72, v70, s94
	v_perm_b32 v70, v72, v70, s68
	v_perm_b32 v72, v73, v71, s94
	v_perm_b32 v71, v73, v71, s68
	v_dot4_i32_i8 v10, v74, v48, v10
	v_dot4_i32_i8 v11, v70, v48, v11
	v_dot4_i32_i8 v8, v72, v48, v8
	v_dot4_i32_i8 v9, v71, v48, v9
	v_and_b32_e32 v73, 0xf0f0f0f0, v74
	v_and_b32_e32 v70, 0xf0f0f0f0, v70
	v_and_b32_e32 v72, 0xf0f0f0f0, v72
	v_and_b32_e32 v71, 0xf0f0f0f0, v71
	v_dot4_i32_i8 v6, v73, v48, v6
	v_dot4_i32_i8 v7, v70, v48, v7
	v_dot4_i32_i8 v4, v72, v48, v4
	v_dot4_i32_i8 v5, v71, v48, v5
	v_dot4_i32_i8 v134, v130, v48, v134

.LvB_t0:
	s_mulk_i32 s2, 0x690
	s_lshr_b32 s3, s5, 17
	s_add_i32 s2, s90, s2
	s_and_b32 s3, s3, 0x7ffc
	s_add_i32 s2, s2, s3
	v_mov_b32_e32 v48, s2
	ds_read_b32 v48, v48 offset:512
	v_perm_b32 v126, v82, v76, s91
	v_perm_b32 v76, v82, v76, s92
	v_perm_b32 v82, v90, v84, s91
	v_perm_b32 v84, v90, v84, s92
	v_perm_b32 v90, v82, v126, s94
	v_perm_b32 v82, v82, v126, s68
	v_perm_b32 v126, v84, v76, s94
	v_perm_b32 v76, v84, v76, s68
	s_waitcnt lgkmcnt(0)
	v_dot4_i32_i8 v54, v90, v48, v54
	v_dot4_i32_i8 v55, v82, v48, v55
	v_dot4_i32_i8 v56, v126, v48, v56
	v_dot4_i32_i8 v57, v76, v48, v57
	v_and_b32_e32 v82, 0xf0f0f0f0, v82
	v_and_b32_e32 v76, 0xf0f0f0f0, v76
	v_and_b32_e32 v84, 0xf0f0f0f0, v90
	v_and_b32_e32 v90, 0xf0f0f0f0, v126
	v_dot4_i32_i8 v58, v84, v48, v58
	v_dot4_i32_i8 v59, v82, v48, v59
	v_dot4_i32_i8 v60, v90, v48, v60
	v_dot4_i32_i8 v61, v76, v48, v61
	v_perm_b32 v76, v83, v77, s91
	v_perm_b32 v82, v91, v85, s91
	v_perm_b32 v77, v83, v77, s92
	v_perm_b32 v83, v91, v85, s92
	v_perm_b32 v84, v82, v76, s94
	v_perm_b32 v76, v82, v76, s68
	v_perm_b32 v82, v83, v77, s94
	v_perm_b32 v77, v83, v77, s68
	v_dot4_i32_i8 v62, v84, v48, v62
	v_dot4_i32_i8 v63, v76, v48, v63
	v_dot4_i32_i8 v64, v82, v48, v64
	v_dot4_i32_i8 v65, v77, v48, v65
	v_and_b32_e32 v83, 0xf0f0f0f0, v84
	v_and_b32_e32 v76, 0xf0f0f0f0, v76
	v_and_b32_e32 v82, 0xf0f0f0f0, v82
	v_and_b32_e32 v77, 0xf0f0f0f0, v77
	v_dot4_i32_i8 v66, v83, v48, v66
	v_dot4_i32_i8 v67, v76, v48, v67
	v_dot4_i32_i8 v68, v82, v48, v68
	v_dot4_i32_i8 v69, v77, v48, v69
	v_dot4_i32_i8 v131, v130, v48, v131
	s_branch .LBB0_2881
.LvB_t1:
	s_mulk_i32 s2, 0x690
	s_lshr_b32 s3, s5, 17
	s_add_i32 s2, s90, s2
	s_and_b32 s3, s3, 0x7ffc
	s_add_i32 s2, s2, s3
	v_mov_b32_e32 v48, s2
	ds_read_b32 v48, v48 offset:512
	v_perm_b32 v126, v82, v76, s91
	v_perm_b32 v76, v82, v76, s92
	v_perm_b32 v82, v90, v84, s91
	v_perm_b32 v84, v90, v84, s92
	v_perm_b32 v90, v82, v126, s94
	v_perm_b32 v82, v82, v126, s68
	v_perm_b32 v126, v84, v76, s94
	v_perm_b32 v76, v84, v76, s68
	s_waitcnt lgkmcnt(0)
	v_dot4_i32_i8 v36, v90, v48, v36
	v_dot4_i32_i8 v37, v82, v48, v37
	v_dot4_i32_i8 v38, v126, v48, v38
	v_dot4_i32_i8 v39, v76, v48, v39
	v_and_b32_e32 v82, 0xf0f0f0f0, v82
	v_and_b32_e32 v76, 0xf0f0f0f0, v76
	v_and_b32_e32 v84, 0xf0f0f0f0, v90
	v_and_b32_e32 v90, 0xf0f0f0f0, v126
	v_dot4_i32_i8 v40, v84, v48, v40
	v_dot4_i32_i8 v41, v82, v48, v41
	v_dot4_i32_i8 v42, v90, v48, v42
	v_dot4_i32_i8 v43, v76, v48, v43
	v_perm_b32 v76, v83, v77, s91
	v_perm_b32 v82, v91, v85, s91
	v_perm_b32 v77, v83, v77, s92
	v_perm_b32 v83, v91, v85, s92
	v_perm_b32 v84, v82, v76, s94
	v_perm_b32 v76, v82, v76, s68
	v_perm_b32 v82, v83, v77, s94
	v_perm_b32 v77, v83, v77, s68
	v_dot4_i32_i8 v44, v84, v48, v44
	v_dot4_i32_i8 v45, v76, v48, v45
	v_dot4_i32_i8 v46, v82, v48, v46
	v_dot4_i32_i8 v47, v77, v48, v47
	v_and_b32_e32 v83, 0xf0f0f0f0, v84
	v_and_b32_e32 v76, 0xf0f0f0f0, v76
	v_and_b32_e32 v82, 0xf0f0f0f0, v82
	v_and_b32_e32 v77, 0xf0f0f0f0, v77
	v_dot4_i32_i8 v50, v83, v48, v50
	v_dot4_i32_i8 v51, v76, v48, v51
	v_dot4_i32_i8 v52, v82, v48, v52
	v_dot4_i32_i8 v53, v77, v48, v53
	v_dot4_i32_i8 v132, v130, v48, v132
	s_branch .LBB0_2881
.LvB_t2:
	s_mulk_i32 s2, 0x690
	s_lshr_b32 s3, s5, 17
	s_add_i32 s2, s90, s2
	s_and_b32 s3, s3, 0x7ffc
	s_add_i32 s2, s2, s3
	v_mov_b32_e32 v48, s2
	ds_read_b32 v48, v48 offset:512
	v_perm_b32 v126, v82, v76, s91
	v_perm_b32 v76, v82, v76, s92
	v_perm_b32 v82, v90, v84, s91
	v_perm_b32 v84, v90, v84, s92
	v_perm_b32 v90, v82, v126, s94
	v_perm_b32 v82, v82, v126, s68
	v_perm_b32 v126, v84, v76, s94
	v_perm_b32 v76, v84, v76, s68
	s_waitcnt lgkmcnt(0)
	v_dot4_i32_i8 v20, v90, v48, v20
	v_dot4_i32_i8 v21, v82, v48, v21
	v_dot4_i32_i8 v22, v126, v48, v22
	v_dot4_i32_i8 v23, v76, v48, v23
	v_and_b32_e32 v82, 0xf0f0f0f0, v82
	v_and_b32_e32 v76, 0xf0f0f0f0, v76
	v_and_b32_e32 v84, 0xf0f0f0f0, v90
	v_and_b32_e32 v90, 0xf0f0f0f0, v126
	v_dot4_i32_i8 v24, v84, v48, v24
	v_dot4_i32_i8 v25, v82, v48, v25
	v_dot4_i32_i8 v26, v90, v48, v26
	v_dot4_i32_i8 v27, v76, v48, v27
	v_perm_b32 v76, v83, v77, s91
	v_perm_b32 v82, v91, v85, s91
	v_perm_b32 v77, v83, v77, s92
	v_perm_b32 v83, v91, v85, s92
	v_perm_b32 v84, v82, v76, s94
	v_perm_b32 v76, v82, v76, s68
	v_perm_b32 v82, v83, v77, s94
	v_perm_b32 v77, v83, v77, s68
	v_dot4_i32_i8 v28, v84, v48, v28
	v_dot4_i32_i8 v29, v76, v48, v29
	v_dot4_i32_i8 v30, v82, v48, v30
	v_dot4_i32_i8 v31, v77, v48, v31
	v_and_b32_e32 v83, 0xf0f0f0f0, v84
	v_and_b32_e32 v76, 0xf0f0f0f0, v76
	v_and_b32_e32 v82, 0xf0f0f0f0, v82
	v_and_b32_e32 v77, 0xf0f0f0f0, v77
	v_dot4_i32_i8 v32, v83, v48, v32
	v_dot4_i32_i8 v33, v76, v48, v33
	v_dot4_i32_i8 v34, v82, v48, v34
	v_dot4_i32_i8 v35, v77, v48, v35
	v_dot4_i32_i8 v133, v130, v48, v133
	s_branch .LBB0_2881
.LvB_t3:
	s_mulk_i32 s2, 0x690
	s_lshr_b32 s3, s5, 17
	s_add_i32 s2, s90, s2
	s_and_b32 s3, s3, 0x7ffc
	s_add_i32 s2, s2, s3
	v_mov_b32_e32 v48, s2
	ds_read_b32 v48, v48 offset:512
	v_perm_b32 v126, v82, v76, s91
	v_perm_b32 v76, v82, v76, s92
	v_perm_b32 v82, v90, v84, s91
	v_perm_b32 v84, v90, v84, s92
	v_perm_b32 v90, v82, v126, s94
	v_perm_b32 v82, v82, v126, s68
	v_perm_b32 v126, v84, v76, s94
	v_perm_b32 v76, v84, v76, s68
	s_waitcnt lgkmcnt(0)
	v_dot4_i32_i8 v18, v90, v48, v18
	v_dot4_i32_i8 v19, v82, v48, v19
	v_dot4_i32_i8 v16, v126, v48, v16
	v_dot4_i32_i8 v17, v76, v48, v17
	v_and_b32_e32 v82, 0xf0f0f0f0, v82
	v_and_b32_e32 v76, 0xf0f0f0f0, v76
	v_and_b32_e32 v84, 0xf0f0f0f0, v90
	v_and_b32_e32 v90, 0xf0f0f0f0, v126
	v_dot4_i32_i8 v14, v84, v48, v14
	v_dot4_i32_i8 v15, v82, v48, v15
	v_dot4_i32_i8 v12, v90, v48, v12
	v_dot4_i32_i8 v13, v76, v48, v13
	v_perm_b32 v76, v83, v77, s91
	v_perm_b32 v82, v91, v85, s91
	v_perm_b32 v77, v83, v77, s92
	v_perm_b32 v83, v91, v85, s92
	v_perm_b32 v84, v82, v76, s94
	v_perm_b32 v76, v82, v76, s68
	v_perm_b32 v82, v83, v77, s94
	v_perm_b32 v77, v83, v77, s68
	v_dot4_i32_i8 v10, v84, v48, v10
	v_dot4_i32_i8 v11, v76, v48, v11
	v_dot4_i32_i8 v8, v82, v48, v8
	v_dot4_i32_i8 v9, v77, v48, v9
	v_and_b32_e32 v83, 0xf0f0f0f0, v84
	v_and_b32_e32 v76, 0xf0f0f0f0, v76
	v_and_b32_e32 v82, 0xf0f0f0f0, v82
	v_and_b32_e32 v77, 0xf0f0f0f0, v77
	v_dot4_i32_i8 v6, v83, v48, v6
	v_dot4_i32_i8 v7, v76, v48, v7
	v_dot4_i32_i8 v4, v82, v48, v4
	v_dot4_i32_i8 v5, v77, v48, v5
	v_dot4_i32_i8 v134, v130, v48, v134
